# v52 + spatial gating unit: first k-step blocks also read all four fragment pairs up front (temp quads, counted waits)
# baseline (speedup 1.0000x reference)
; #define LAS __attribute__((address_space(3)))
; __device__ __forceinline__ void sgu_unit(LAS unsigned char* lds, int unit, const bf16* U, const bf16* VG, const bf16* Wsb, const float* bs, const float* lng, const float* lnb, bf16* YA, const float* stat, int tid_in, int lane_in, int wave, unsigned* probe_words = nullptr) {
;     ...
;             for (int kk = 0; kk < 4; ++kk) if (kk <= (wave >> 1)) {
; #pragma unroll
;                 for (int nn = 0; nn < 4; ++nn) { const LAS unsigned char* ap = tb + kk * (32 * 512) + (((gi * 8 + nn * 2) ^ xkp) * 16);
;                     const s16x4s lo = __builtin_bit_cast(s16x4s, __builtin_amdgcn_ds_read_tr16_b64_v4i16((LAS s16x4s*)ap)), hi = __builtin_bit_cast(s16x4s, __builtin_amdgcn_ds_read_tr16_b64_v4i16((LAS s16x4s*)(ap + 4 * 512)));
;                     const bf16x8 vf = {lo[0], lo[1], lo[2], lo[3], hi[0], hi[1], hi[2], hi[3]};
;                     acc[nn] = __builtin_amdgcn_mfma_f32_16x16x32_bf16(vf, wf[gi][kk], acc[nn], 0, 0, 0); }
;             }
.LBB0_1016:
	ds_read_b64_tr_b16 v[156:157], v124 offset:4096
	ds_read_b64_tr_b16 v[158:159], v124 offset:6144
	ds_read_b64_tr_b16 v[144:145], v123 offset:4096
	ds_read_b64_tr_b16 v[146:147], v123 offset:6144
	ds_read_b64_tr_b16 v[148:149], v122 offset:4096
	ds_read_b64_tr_b16 v[150:151], v122 offset:6144
	ds_read_b64_tr_b16 v[152:153], v2 offset:4096
	ds_read_b64_tr_b16 v[154:155], v2 offset:6144
	s_waitcnt lgkmcnt(6)
	v_mfma_f32_16x16x32_bf16 v[76:79], v[156:159], v[64:67], 0
	s_waitcnt lgkmcnt(4)
	v_mfma_f32_16x16x32_bf16 v[72:75], v[144:147], v[64:67], 0
	s_waitcnt lgkmcnt(0)
	v_mfma_f32_16x16x32_bf16 v[84:87], v[152:155], v[64:67], 0
	v_mfma_f32_16x16x32_bf16 v[68:71], v[148:151], v[64:67], 0
	s_nop 6
	v_mov_b32_e32 v80, v84
	v_mov_b32_e32 v81, v85
	v_mov_b32_e32 v82, v86
	v_mov_b32_e32 v83, v87
	s_and_b64 vcc, exec, s[8:9]
	s_cbranch_vccnz .LBB0_995

; #define LAS __attribute__((address_space(3)))
; __device__ __forceinline__ void sgu_unit(LAS unsigned char* lds, int unit, const bf16* U, const bf16* VG, const bf16* Wsb, const float* bs, const float* lng, const float* lnb, bf16* YA, const float* stat, int tid_in, int lane_in, int wave, unsigned* probe_words = nullptr) {
;     ...
;             for (int kk = 0; kk < 4; ++kk) if (kk <= (wave >> 1)) {
; #pragma unroll
;                 for (int nn = 0; nn < 4; ++nn) { const LAS unsigned char* ap = tb + kk * (32 * 512) + (((gi * 8 + nn * 2) ^ xkp) * 16);
;                     const s16x4s lo = __builtin_bit_cast(s16x4s, __builtin_amdgcn_ds_read_tr16_b64_v4i16((LAS s16x4s*)ap)), hi = __builtin_bit_cast(s16x4s, __builtin_amdgcn_ds_read_tr16_b64_v4i16((LAS s16x4s*)(ap + 4 * 512)));
;                     const bf16x8 vf = {lo[0], lo[1], lo[2], lo[3], hi[0], hi[1], hi[2], hi[3]};
;                     acc[nn] = __builtin_amdgcn_mfma_f32_16x16x32_bf16(vf, wf[gi][kk], acc[nn], 0, 0, 0); }
;             }
.LBB0_1019:
	ds_read_b64_tr_b16 v[156:157], v75 offset:4096
	ds_read_b64_tr_b16 v[158:159], v75 offset:6144
	ds_read_b64_tr_b16 v[144:145], v74 offset:4096
	ds_read_b64_tr_b16 v[146:147], v74 offset:6144
	ds_read_b64_tr_b16 v[148:149], v73 offset:4096
	ds_read_b64_tr_b16 v[150:151], v73 offset:6144
	ds_read_b64_tr_b16 v[152:153], v72 offset:4096
	ds_read_b64_tr_b16 v[154:155], v72 offset:6144
	s_waitcnt lgkmcnt(6)
	v_mfma_f32_16x16x32_bf16 v[60:63], v[156:159], v[48:51], 0
	s_waitcnt lgkmcnt(4)
	v_mfma_f32_16x16x32_bf16 v[56:59], v[144:147], v[48:51], 0
	s_waitcnt lgkmcnt(0)
	v_mfma_f32_16x16x32_bf16 v[68:71], v[152:155], v[48:51], 0
	v_mfma_f32_16x16x32_bf16 v[52:55], v[148:151], v[48:51], 0
	s_nop 6
	v_mov_b32_e32 v64, v68
	v_mov_b32_e32 v65, v69
	v_mov_b32_e32 v66, v70
	v_mov_b32_e32 v67, v71
	s_and_b64 vcc, exec, s[8:9]
	s_cbranch_vccnz .LBB0_1000

; #define LAS __attribute__((address_space(3)))
; __device__ __forceinline__ void sgu_unit(LAS unsigned char* lds, int unit, const bf16* U, const bf16* VG, const bf16* Wsb, const float* bs, const float* lng, const float* lnb, bf16* YA, const float* stat, int tid_in, int lane_in, int wave, unsigned* probe_words = nullptr) {
;     ...
;             for (int kk = 0; kk < 4; ++kk) if (kk <= (wave >> 1)) {
; #pragma unroll
;                 for (int nn = 0; nn < 4; ++nn) { const LAS unsigned char* ap = tb + kk * (32 * 512) + (((gi * 8 + nn * 2) ^ xkp) * 16);
;                     const s16x4s lo = __builtin_bit_cast(s16x4s, __builtin_amdgcn_ds_read_tr16_b64_v4i16((LAS s16x4s*)ap)), hi = __builtin_bit_cast(s16x4s, __builtin_amdgcn_ds_read_tr16_b64_v4i16((LAS s16x4s*)(ap + 4 * 512)));
;                     const bf16x8 vf = {lo[0], lo[1], lo[2], lo[3], hi[0], hi[1], hi[2], hi[3]};
;                     acc[nn] = __builtin_amdgcn_mfma_f32_16x16x32_bf16(vf, wf[gi][kk], acc[nn], 0, 0, 0); }
;             }
.LBB0_1022:
	ds_read_b64_tr_b16 v[156:157], v124 offset:4352
	ds_read_b64_tr_b16 v[158:159], v124 offset:6400
	ds_read_b64_tr_b16 v[144:145], v123 offset:4352
	ds_read_b64_tr_b16 v[146:147], v123 offset:6400
	ds_read_b64_tr_b16 v[148:149], v122 offset:4352
	ds_read_b64_tr_b16 v[150:151], v122 offset:6400
	ds_read_b64_tr_b16 v[152:153], v2 offset:4352
	ds_read_b64_tr_b16 v[154:155], v2 offset:6400
	s_waitcnt lgkmcnt(6)
	v_mfma_f32_16x16x32_bf16 v[44:47], v[156:159], v[32:35], 0
	s_waitcnt lgkmcnt(4)
	v_mfma_f32_16x16x32_bf16 v[40:43], v[144:147], v[32:35], 0
	s_waitcnt lgkmcnt(0)
	v_mfma_f32_16x16x32_bf16 v[52:55], v[152:155], v[32:35], 0
	v_mfma_f32_16x16x32_bf16 v[36:39], v[148:151], v[32:35], 0
	s_nop 6
	v_mov_b32_e32 v48, v52
	v_mov_b32_e32 v49, v53
	v_mov_b32_e32 v50, v54
	v_mov_b32_e32 v51, v55
	s_and_b64 vcc, exec, s[8:9]
	s_cbranch_vccnz .LBB0_1005

; #define LAS __attribute__((address_space(3)))
; __device__ __forceinline__ void sgu_unit(LAS unsigned char* lds, int unit, const bf16* U, const bf16* VG, const bf16* Wsb, const float* bs, const float* lng, const float* lnb, bf16* YA, const float* stat, int tid_in, int lane_in, int wave, unsigned* probe_words = nullptr) {
;     ...
;             for (int kk = 0; kk < 4; ++kk) if (kk <= (wave >> 1)) {
; #pragma unroll
;                 for (int nn = 0; nn < 4; ++nn) { const LAS unsigned char* ap = tb + kk * (32 * 512) + (((gi * 8 + nn * 2) ^ xkp) * 16);
;                     const s16x4s lo = __builtin_bit_cast(s16x4s, __builtin_amdgcn_ds_read_tr16_b64_v4i16((LAS s16x4s*)ap)), hi = __builtin_bit_cast(s16x4s, __builtin_amdgcn_ds_read_tr16_b64_v4i16((LAS s16x4s*)(ap + 4 * 512)));
;                     const bf16x8 vf = {lo[0], lo[1], lo[2], lo[3], hi[0], hi[1], hi[2], hi[3]};
;                     acc[nn] = __builtin_amdgcn_mfma_f32_16x16x32_bf16(vf, wf[gi][kk], acc[nn], 0, 0, 0); }
;             }
.LBB0_1025:
	ds_read_b64_tr_b16 v[156:157], v75 offset:4352
	ds_read_b64_tr_b16 v[158:159], v75 offset:6400
	ds_read_b64_tr_b16 v[144:145], v74 offset:4352
	ds_read_b64_tr_b16 v[146:147], v74 offset:6400
	ds_read_b64_tr_b16 v[148:149], v73 offset:4352
	ds_read_b64_tr_b16 v[150:151], v73 offset:6400
	ds_read_b64_tr_b16 v[152:153], v72 offset:4352
	ds_read_b64_tr_b16 v[154:155], v72 offset:6400
	s_waitcnt lgkmcnt(6)
	v_mfma_f32_16x16x32_bf16 v[28:31], v[156:159], v[16:19], 0
	s_waitcnt lgkmcnt(4)
	v_mfma_f32_16x16x32_bf16 v[24:27], v[144:147], v[16:19], 0
	s_waitcnt lgkmcnt(0)
	v_mfma_f32_16x16x32_bf16 v[36:39], v[152:155], v[16:19], 0
	v_mfma_f32_16x16x32_bf16 v[20:23], v[148:151], v[16:19], 0
	s_nop 6
	v_mov_b32_e32 v32, v36
	v_mov_b32_e32 v33, v37
	v_mov_b32_e32 v34, v38
	v_mov_b32_e32 v35, v39
	s_and_b64 vcc, exec, s[8:9]
	s_cbranch_vccnz .LBB0_1010
